# speedup vs baseline: 1.0124x; 1.0124x over previous
_Z9fast_mainILb0EEvPKiS1_S1_PKfPKcS3_PfS6_PiPyS6_:
	s_nop 0
	s_load_dwordx4 s[4:7], s[0:1], 0x20
	s_load_dwordx4 s[8:11], s[0:1], 0x8
	s_load_dwordx2 s[16:17], s[0:1], 0x0
	v_and_b32_e32 v1, 63, v0
	v_lshrrev_b32_e32 v8, 6, v0
	v_lshlrev_b32_e32 v150, 4, v1
	v_lshl_or_b32 v14, s2, 3, v8
	v_lshlrev_b32_e32 v14, 10, v14
	v_or_b32_e32 v14, v14, v150
	v_add_u32_e32 v212, 0x10000, v150
	v_add_u32_e32 v213, 0x18c00, v150
	v_mov_b32_e32 v151, 0
	s_waitcnt lgkmcnt(0)
	v_lshl_add_u64 v[4:5], s[4:5], 0, v[150:151]
	v_lshlrev_b32_e32 v2, 10, v8
	v_mov_b32_e32 v3, v151
	v_lshl_add_u64 v[6:7], v[4:5], 0, v[2:3]
	v_readfirstlane_b32 s3, v2
	v_or_b32_e32 v3, 0x2000, v2
	s_mov_b32 m0, s3
	s_mov_b64 s[4:5], 0x2000
	v_readfirstlane_b32 s3, v3
	global_load_lds_dwordx4 v[6:7], off
	v_lshl_add_u64 v[10:11], v[6:7], 0, s[4:5]
	s_mov_b32 m0, s3
	v_or_b32_e32 v3, 0x6000, v2
	global_load_lds_dwordx4 v[10:11], off
	v_or_b32_e32 v10, 0x4000, v2
	v_mov_b32_e32 v11, v151
	v_readfirstlane_b32 s3, v10
	v_lshl_add_u64 v[12:13], v[4:5], 0, v[10:11]
	s_mov_b32 m0, s3
	s_mov_b64 s[4:5], 0x6000
	v_readfirstlane_b32 s3, v3
	global_load_lds_dwordx4 v[12:13], off
	v_lshl_add_u64 v[10:11], v[6:7], 0, s[4:5]
	s_mov_b32 m0, s3
	v_or_b32_e32 v3, 0xa000, v2
	global_load_lds_dwordx4 v[10:11], off
	v_or_b32_e32 v10, 0x8000, v2
	v_mov_b32_e32 v11, v151
	v_readfirstlane_b32 s3, v10
	v_lshl_add_u64 v[12:13], v[4:5], 0, v[10:11]
	s_mov_b32 m0, s3
	s_mov_b64 s[4:5], 0xa000
	v_readfirstlane_b32 s3, v3
	global_load_lds_dwordx4 v[12:13], off
	v_or_b32_e32 v26, 0x60, v8
	s_movk_i32 s18, 0x63
	v_cmp_gt_u32_e32 vcc, s18, v26
	s_and_saveexec_b64 s[12:13], vcc
	s_cbranch_execz .Ld13_skip
	v_lshlrev_b32_e32 v26, 10, v26
	v_mov_b32_e32 v27, 0
	v_readfirstlane_b32 s18, v26
	v_lshl_add_u64 v[24:25], v[4:5], 0, v[26:27]
	s_mov_b32 m0, s18
	s_nop 0
	global_load_lds_dwordx4 v[24:25], off
